# expert-weight transposes: the w1/w3 base pointers are read from the kernarg segment once before the work-queue loop instead of an s_load + lgkmcnt(0) for every tile (4 per batch)
# speedup vs baseline: 1.0151x; 1.0026x over previous
; __device__ __forceinline__ TrJob tr_job(const Params& p, int id) {
;     if (id < TR_WIN) { const int nt = id / 32, kt = id % 32; return TrJob{p.w_in, NIN, nt * 64, kt * 64, (bf16_t*)(p.ws + WS_WINT) + (size_t)nt * 64 * DM, DM, nullptr, nullptr, nullptr, nullptr}; }
;     id -= TR_WIN;
;     if (id < 4 * TR_SQ) { const int w4 = id / TR_SQ, w = w4 == 0 ? 0 : w4 + 1, r = id % TR_SQ, nt = r / 32, kt = r % 32;
;         const float* src = w == 0 ? p.w_out : w == 2 ? p.wk : w == 3 ? p.wv : p.wo;
;         TrJob j{src, DM, nt * 64, kt * 64, (bf16_t*)(p.ws + WS_WOUTT + (size_t)w * 8 * MiB) + (size_t)nt * 64 * DM, DM, nullptr, nullptr, nullptr, nullptr};
;         return j; }
;     id -= 4 * TR_SQ;
;     if (id < TR_W13) { const int e = id / 512, r = id % 512, ntile = r / 32, kt = r % 32, n0 = ntile * 64, pn = n0 / 256, rr = n0 % 256;
;         const float* src = (rr < 128 ? p.w1 : p.w3) + (size_t)e * DM * 512;
;         return TrJob{src, 512, pn * 128 + (rr & 127), kt * 64, (bf16_t*)(p.ws + WS_W13T) + ((size_t)e * 1024 + n0) * DM, DM, p.ln2_g, p.ln2_b, (float*)(p.ws + WS_G13) + (size_t)e * 1024 + n0, (float*)(p.ws + WS_B13) + (size_t)e * 1024 + n0}; }
; __device__ __forceinline__ void ph_transpose_experts(const Params& p, LAS unsigned char* lds, LAS unsigned char* xl) {
;     ...
;     __syncthreads();
;     if (tid == 0) { sh[0] = (int)atomicAdd(ctr, 1u); sh[1] = (int)atomicAdd(ctr, 1u); }
;     __syncthreads();
;     int s = __builtin_amdgcn_readfirstlane(sh[0]), par = 0, bi = 0, claimed = NS;
;     if (s >= NS) return;
;     f32x4 v[4][2], vn[4][2]; float gs[4][2], bs[4][2], gsn[4][2], bsn[4][2];
;     ...
;     TRX_LOAD(s, 0, v, gs, bs);
.LBB0_476:
	s_or_b64 exec, exec, s[10:11]
	s_add_i32 s67, 0, 0x20000
	v_mov_b32_e32 v1, s67
	s_waitcnt lgkmcnt(0)
	s_barrier
	ds_read_b32 v1, v1
	s_mov_b32 s11, 0
	s_waitcnt lgkmcnt(0)
	v_readfirstlane_b32 s4, v1
	s_cmpk_gt_i32 s4, 0xbff
	s_cbranch_scc1 .LBB0_661
	s_lshl_b32 s0, s4, 5
	s_add_i32 s2, s0, 0x1c00
	s_lshl_b32 s0, s4, 3
	s_add_i32 s3, s0, 0x7c00
	s_cmpk_lt_i32 s4, 0x400
	s_cselect_b64 s[34:35], -1, 0
	s_and_b64 s[0:1], s[34:35], exec
	s_load_dwordx2 s[0:1], s[70:71], 0xb8
	s_cselect_b32 s5, s2, s3
	s_add_i32 s2, s5, 0xffff6400
	s_lshr_b32 s10, s2, 8
	s_lshl_b64 s[2:3], s[10:11], 22
	s_waitcnt lgkmcnt(0)
	s_add_u32 s16, s0, s2
	s_addc_u32 s17, s1, s3
	s_lshl_b32 s0, s5, 3
	s_and_b32 s18, s0, 0x7c0
	s_add_i32 s0, s5, 0xffffe400
	s_lshr_b32 s10, s0, 9
	s_lshl_b32 s6, s5, 1
	s_and_b32 s7, s5, 64
	s_add_u32 s0, s70, 0xa8
	s_addc_u32 s1, s71, 0
	s_add_u32 s2, s70, 0xb0
	s_addc_u32 s3, s71, 0
	s_load_dwordx4 s[12:15], s[70:71], 0x88
	s_load_dwordx2 s[30:31], s[70:71], 0x20
	s_load_dwordx2 s[98:99], s[70:71], 0xa8
	s_load_dwordx2 s[100:101], s[70:71], 0xb0
	s_waitcnt lgkmcnt(0)
	s_cmp_eq_u32 s7, 0
	s_cselect_b32 s29, s1, s3
	s_cselect_b32 s28, s0, s2
	s_lshl_b64 s[22:23], s[10:11], 22
	s_and_b32 s7, s5, 0x180
	s_and_b32 s10, s6, 64
	s_or_b32 s7, s10, s7
	s_and_b32 s6, s6, 0x7c0
	s_cmpk_gt_i32 s5, 0xbff
	s_cbranch_scc0 .LBB0_481
	s_cmpk_gt_u32 s5, 0x1bff
	s_cbranch_scc0 .LBB0_482
	s_cmpk_gt_u32 s5, 0x9bff
	s_mov_b64 s[44:45], 0
	s_cbranch_scc1 .LBB0_706
	s_load_dwordx2 s[10:11], s[28:29], 0x0
	s_lshl_b32 s19, s5, 6
	s_and_b32 s19, s19, 0x600
	s_mov_b64 s[40:41], 0x200
	s_waitcnt lgkmcnt(0)
	s_mov_b64 s[36:37], s[14:15]
	s_add_u32 s10, s10, s22
	s_addc_u32 s11, s11, s23
	s_mov_b64 s[38:39], s[12:13]
	s_mov_b32 s42, s7
	s_andn2_b64 vcc, exec, s[44:45]
	s_cbranch_vccz .LBB0_483
	s_branch .LBB0_484

; __device__ __forceinline__ TrJob tr_job(const Params& p, int id) {
;     ...
;     if (id < TR_W13) { const int e = id / 512, r = id % 512, ntile = r / 32, kt = r % 32, n0 = ntile * 64, pn = n0 / 256, rr = n0 % 256;
;         const float* src = (rr < 128 ? p.w1 : p.w3) + (size_t)e * DM * 512;
;         return TrJob{src, 512, pn * 128 + (rr & 127), kt * 64, (bf16_t*)(p.ws + WS_W13T) + ((size_t)e * 1024 + n0) * DM, DM, p.ln2_g, p.ln2_b, (float*)(p.ws + WS_G13) + (size_t)e * 1024 + n0, (float*)(p.ws + WS_B13) + (size_t)e * 1024 + n0}; }
.LBB0_544:
	s_mov_b64 s[50:51], 0x800
	s_andn2_b64 vcc, exec, s[14:15]
	s_mov_b64 s[52:53], s[48:49]
	s_mov_b32 s54, s40
	s_mov_b64 s[14:15], s[38:39]
	s_cbranch_vccnz .LBB0_546
	s_cmp_eq_u32 s44, s0
	s_cselect_b32 s14, s98, s100
	s_cselect_b32 s15, s99, s101
	s_mov_b64 s[50:51], 0x200
	s_waitcnt lgkmcnt(0)
	s_mov_b64 s[52:53], s[18:19]
	s_add_u32 s14, s14, s42
	s_addc_u32 s15, s15, s43
	s_lshl_b32 s54, s41, 6
	s_and_b32 s55, s54, 0x700
	s_mov_b32 s54, s65

; __device__ __forceinline__ TrJob tr_job(const Params& p, int id) {
;     ...
;     if (id < TR_W13) { const int e = id / 512, r = id % 512, ntile = r / 32, kt = r % 32, n0 = ntile * 64, pn = n0 / 256, rr = n0 % 256;
;         const float* src = (rr < 128 ? p.w1 : p.w3) + (size_t)e * DM * 512;
;         return TrJob{src, 512, pn * 128 + (rr & 127), kt * 64, (bf16_t*)(p.ws + WS_W13T) + ((size_t)e * 1024 + n0) * DM, DM, p.ln2_g, p.ln2_b, (float*)(p.ws + WS_G13) + (size_t)e * 1024 + n0, (float*)(p.ws + WS_B13) + (size_t)e * 1024 + n0}; }
.LBB0_561:
	s_mov_b64 s[48:49], 0x800
	s_andn2_b64 vcc, exec, s[50:51]
	s_mov_b64 s[50:51], s[46:47]
	s_mov_b32 s54, s40
	s_mov_b64 s[52:53], s[38:39]
	s_cbranch_vccnz .LBB0_563
	s_cmp_eq_u32 s44, s0
	s_cselect_b32 s52, s98, s100
	s_cselect_b32 s53, s99, s101
	s_mov_b64 s[48:49], 0x200
	s_mov_b64 s[50:51], s[18:19]
	s_waitcnt lgkmcnt(0)
	s_add_u32 s52, s52, s42
	s_addc_u32 s53, s53, s43
	s_lshl_b32 s54, s55, 6
	s_and_b32 s66, s54, 0x7c0
	s_mov_b32 s54, s65

; __device__ __forceinline__ TrJob tr_job(const Params& p, int id) {
;     ...
;     if (id < TR_W13) { const int e = id / 512, r = id % 512, ntile = r / 32, kt = r % 32, n0 = ntile * 64, pn = n0 / 256, rr = n0 % 256;
;         const float* src = (rr < 128 ? p.w1 : p.w3) + (size_t)e * DM * 512;
;         return TrJob{src, 512, pn * 128 + (rr & 127), kt * 64, (bf16_t*)(p.ws + WS_W13T) + ((size_t)e * 1024 + n0) * DM, DM, p.ln2_g, p.ln2_b, (float*)(p.ws + WS_G13) + (size_t)e * 1024 + n0, (float*)(p.ws + WS_B13) + (size_t)e * 1024 + n0}; }
.LBB0_595:
	s_cmp_eq_u32 s44, s0
	s_cselect_b32 s38, s98, s100
	s_cselect_b32 s39, s99, s101
	s_mov_b64 s[48:49], 0x200
	s_mov_b64 s[50:51], s[18:19]
	s_waitcnt lgkmcnt(0)
	s_add_u32 s38, s38, s42
	s_addc_u32 s39, s39, s43
	s_lshl_b32 s40, s54, 6
	s_and_b32 s55, s40, 0x7c0
	s_mov_b32 s40, s65
